# spare-XCD layer-1 conversion with guard: if fewer than 3 XCD groups are lightly loaded all workgroups share the conversion
# speedup vs baseline: 1.0151x; 1.0151x over previous
; #define WSP(type, off) ((type*)(KWS() + (off)))
; #define SEAM(k) do { if (IN(k) && IN((k) + 1)) GRID_BAR(); } while (0)
;     __device__ bool next(int i, Unit& u) const {
;     ...
;         if (aligned) {
;             const int ng = (nM + WGM - 1) / WGM, gq = ng / NXCD, gr = ng % NXCD, xcd = (int)(L % NXCD); const long off = L / NXCD;
;             const int g0 = xcd * gq + (xcd < gr ? xcd : gr), g1 = g0 + gq + (xcd < gr ? 1 : 0);
;             const long w = (long)g0 * (WGM * 4) + off, wend = (long)g1 * (WGM * 4) < nwg ? (long)g1 * (WGM * 4) : nwg;
;             if (w >= wend) return false;
;             wgid = (int)w;
; __global__ void __launch_bounds__(NWAVES * 64, 2) mk_fwd(Args args) {
;     ...
;         for (int rep_ = 0; rep_ < REPS(7); ++rep_) if (IN(pb0 + 2)) { bf16_t* act = WSP(bf16_t, WS_ACT); bf16_t* WDN = WSP(bf16_t, WS_WDN); bf16_t* yw = WSP(bf16_t, WS_YW); const float* lw = WSP(float, WS_LW);
;             pg8::Gemm g{act, WDN + (size_t)l * 32 * 1024 * 512, 0, 0, 512}; pg8::MoeOrder S; S.init(rb[32] / 256, G, bid, rb, LOCAL_OK()); pg8::EpiDown E{yw, lw, rb};
;             pg8::gemm_phase<pg8::EpiDown, pg8::MoeOrder, pg8::APlain, true, true>(lds, g, S, E, pg8::APlain{}, wave); }
;         SEAM(pb0 + 2);
.LBB0_1657:
	s_waitcnt vmcnt(0) lgkmcnt(0)
	s_barrier
	v_mov_b32_e32 v252, 0x27c80
	ds_read_b32 v252, v252
	s_waitcnt lgkmcnt(0)
	v_readfirstlane_b32 s100, v252
	s_nop 1
	s_lshr_b32 s100, s100, 8
	s_add_i32 s100, s100, 3
	s_lshr_b32 s100, s100, 2
	s_and_b32 s100, s100, 7
	s_and_b32 s98, s83, 7
	s_cmp_eq_u32 s100, 0
	s_cbranch_scc1 .Lsp_all
	s_cmp_ge_u32 s100, 6
	s_cbranch_scc1 .Lsp_all
	s_cmp_lt_u32 s98, s100
	s_cbranch_scc1 .Lq_done
	s_sub_i32 s98, s98, s100
	s_lshl_b32 s98, s98, 5
	s_lshr_b32 s101, s83, 3
	s_add_i32 s98, s98, s101
	s_sub_i32 s100, 8, s100
	s_lshl_b32 s100, s100, 5
	s_branch .Lsp_go
